# baseline (speedup 1.0000x reference)
_Z11init_kernelPKfS0_S0_S0_PDF16_S1_:
	s_load_dwordx8 s[4:11], s[0:1], 0x0
	s_load_dwordx4 s[12:15], s[0:1], 0x20
	v_readfirstlane_b32 s3, v0
	v_bfe_u32 v32, v0, 4, 2
	v_and_b32_e32 v33, 15, v0
	s_lshr_b32 s3, s3, 6
	s_lshl_b32 s17, s2, 11
	s_lshl_b32 s18, s2, 8
	s_lshl_b32 s19, s3, 7
	s_lshl_b32 s20, s3, 6
	v_mul_u32_u24_e32 v34, 36, v32
	v_lshl_or_b32 v34, v33, 7, v34
	v_mul_u32_u24_e32 v35, 0x900, v32
	v_lshl_or_b32 v35, v33, 2, v35
	v_lshlrev_b32_e32 v36, 2, v33
	v_lshlrev_b32_e32 v37, 4, v0
	v_lshlrev_b32_e32 v42, 9, v32
	v_lshl_or_b32 v42, v33, 1, v42
	v_mov_b32_e32 v44, 0
	v_mov_b32_e32 v45, 0
	v_mov_b32_e32 v46, 0
	v_mov_b32_e32 v47, 0
	v_mov_b32_e32 v39, 0
	v_mov_b32_e32 v41, 0
	v_add_u32_e32 v38, 20, v34
	v_lshlrev_b32_e32 v40, 4, v33
	v_cmp_eq_u32_e32 vcc, 3, v32
	s_waitcnt lgkmcnt(0)
	s_add_u32 s4, s4, s17
	s_addc_u32 s5, s5, 0
	s_add_u32 s6, s6, s18
	s_addc_u32 s7, s7, 0
	s_add_u32 s8, s8, s19
	s_addc_u32 s9, s9, 0
	v_lshl_add_u64 v[38:39], s[4:5], 0, v[38:39]
	v_lshl_add_u64 v[40:41], s[6:7], 0, v[40:41]
	v_cndmask_b32_e32 v38, v38, v40, vcc
	v_cndmask_b32_e32 v39, v39, v41, vcc
	global_load_dwordx4 v[2:5], v34, s[4:5] nt
	global_load_dword v6, v34, s[4:5] offset:16 nt
	global_load_dwordx4 v[8:11], v[38:39], off nt
	global_load_dword v12, v35, s[8:9]
	global_load_dword v21, v35, s[8:9] offset:64
	global_load_dword v13, v35, s[8:9] offset:256
	global_load_dword v22, v35, s[8:9] offset:320
	global_load_dword v14, v35, s[8:9] offset:512
	global_load_dword v23, v35, s[8:9] offset:576
	global_load_dword v15, v35, s[8:9] offset:768
	global_load_dword v24, v35, s[8:9] offset:832
	global_load_dword v16, v35, s[8:9] offset:1024
	global_load_dword v25, v35, s[8:9] offset:1088
	global_load_dword v17, v35, s[8:9] offset:1280
	global_load_dword v26, v35, s[8:9] offset:1344
	global_load_dword v18, v35, s[8:9] offset:1536
	global_load_dword v27, v35, s[8:9] offset:1600
	global_load_dword v19, v35, s[8:9] offset:1792
	global_load_dword v28, v35, s[8:9] offset:1856
	global_load_dword v20, v35, s[8:9] offset:2048
	global_load_dword v29, v35, s[8:9] offset:2112
	s_add_u32 s10, s10, s19
	s_addc_u32 s11, s11, 0
	global_load_dword v30, v36, s[10:11]
	global_load_dword v31, v36, s[10:11] offset:64
	s_add_u32 s14, s14, s17
	s_addc_u32 s15, s15, 0
	s_add_u32 s12, s12, s17
	s_addc_u32 s13, s13, 0
	s_add_u32 s12, s12, s20
	s_addc_u32 s13, s13, 0
	global_load_dword v48, v36, s[12:13]
	global_store_dwordx4 v37, v[44:47], s[14:15]
	v_accvgpr_write_b32 a0, 0
	v_accvgpr_write_b32 a1, 0
	v_accvgpr_write_b32 a2, 0
	v_accvgpr_write_b32 a3, 0
	v_accvgpr_write_b32 a4, 0
	v_accvgpr_write_b32 a5, 0
	v_accvgpr_write_b32 a6, 0
	v_accvgpr_write_b32 a7, 0
	v_and_b32_e32 v43, 1, v0
	s_waitcnt vmcnt(22)
	s_waitcnt vmcnt(20)
	v_mfma_f32_16x16x4_f32 a[0:3], v2, v12, a[0:3]
	v_mfma_f32_16x16x4_f32 a[4:7], v2, v21, a[4:7]
	s_waitcnt vmcnt(18)
	v_mfma_f32_16x16x4_f32 a[0:3], v3, v13, a[0:3]
	v_mfma_f32_16x16x4_f32 a[4:7], v3, v22, a[4:7]
	s_waitcnt vmcnt(16)
	v_mfma_f32_16x16x4_f32 a[0:3], v4, v14, a[0:3]
	v_mfma_f32_16x16x4_f32 a[4:7], v4, v23, a[4:7]
	s_waitcnt vmcnt(14)
	v_mfma_f32_16x16x4_f32 a[0:3], v5, v15, a[0:3]
	v_mfma_f32_16x16x4_f32 a[4:7], v5, v24, a[4:7]
	s_waitcnt vmcnt(12)
	v_mfma_f32_16x16x4_f32 a[0:3], v6, v16, a[0:3]
	v_mfma_f32_16x16x4_f32 a[4:7], v6, v25, a[4:7]
	s_waitcnt vmcnt(10)
	v_mfma_f32_16x16x4_f32 a[0:3], v8, v17, a[0:3]
	v_mfma_f32_16x16x4_f32 a[4:7], v8, v26, a[4:7]
	s_waitcnt vmcnt(8)
	v_mfma_f32_16x16x4_f32 a[0:3], v9, v18, a[0:3]
	v_mfma_f32_16x16x4_f32 a[4:7], v9, v27, a[4:7]
	s_waitcnt vmcnt(6)
	v_mfma_f32_16x16x4_f32 a[0:3], v10, v19, a[0:3]
	v_mfma_f32_16x16x4_f32 a[4:7], v10, v28, a[4:7]
	s_waitcnt vmcnt(4)
	v_mfma_f32_16x16x4_f32 a[0:3], v11, v20, a[0:3]
	v_mfma_f32_16x16x4_f32 a[4:7], v11, v29, a[4:7]
	v_cmp_eq_u32_e32 vcc, 0, v43
	s_waitcnt vmcnt(2)
	s_nop 7
	v_accvgpr_read_b32 v2, a0
	v_accvgpr_read_b32 v3, a1
	v_accvgpr_read_b32 v4, a2
	v_accvgpr_read_b32 v5, a3
	v_accvgpr_read_b32 v6, a4
	v_accvgpr_read_b32 v7, a5
	v_accvgpr_read_b32 v8, a6
	v_accvgpr_read_b32 v9, a7
	v_add_f32_e32 v2, v30, v2
	v_add_f32_e32 v3, v30, v3
	v_add_f32_e32 v4, v30, v4
	v_add_f32_e32 v5, v30, v5
	v_add_f32_e32 v6, v31, v6
	v_add_f32_e32 v7, v31, v7
	v_add_f32_e32 v8, v31, v8
	v_add_f32_e32 v9, v31, v9
	v_mov_b32_dpp v50, v2 quad_perm:[1,0,3,2] row_mask:0xf bank_mask:0xf
	v_mov_b32_dpp v51, v3 quad_perm:[1,0,3,2] row_mask:0xf bank_mask:0xf
	v_mov_b32_dpp v52, v4 quad_perm:[1,0,3,2] row_mask:0xf bank_mask:0xf
	v_mov_b32_dpp v53, v5 quad_perm:[1,0,3,2] row_mask:0xf bank_mask:0xf
	v_mov_b32_dpp v54, v6 quad_perm:[1,0,3,2] row_mask:0xf bank_mask:0xf
	v_mov_b32_dpp v55, v7 quad_perm:[1,0,3,2] row_mask:0xf bank_mask:0xf
	v_mov_b32_dpp v56, v8 quad_perm:[1,0,3,2] row_mask:0xf bank_mask:0xf
	v_mov_b32_dpp v57, v9 quad_perm:[1,0,3,2] row_mask:0xf bank_mask:0xf
	v_cvt_pk_f16_f32 v2, v2, v50
	v_cvt_pk_f16_f32 v3, v3, v51
	v_cvt_pk_f16_f32 v4, v4, v52
	v_cvt_pk_f16_f32 v5, v5, v53
	v_cvt_pk_f16_f32 v6, v6, v54
	v_cvt_pk_f16_f32 v7, v7, v55
	v_cvt_pk_f16_f32 v8, v8, v56
	v_cvt_pk_f16_f32 v9, v9, v57
	s_and_saveexec_b64 s[2:3], vcc
	global_store_dword v42, v2, s[12:13]
	global_store_dword v42, v6, s[12:13] offset:32
	global_store_dword v42, v3, s[12:13] offset:128
	global_store_dword v42, v7, s[12:13] offset:160
	global_store_dword v42, v4, s[12:13] offset:256
	global_store_dword v42, v8, s[12:13] offset:288
	global_store_dword v42, v5, s[12:13] offset:384
	global_store_dword v42, v9, s[12:13] offset:416
	s_endpgm
	.p2align	8

_Z12final_kernelPKDF16_S0_PKfS2_S2_S2_Pf:
	s_load_dwordx8 s[4:11], s[0:1], 0x0
	s_load_dwordx2 s[14:15], s[0:1], 0x20
	s_load_dwordx4 s[16:19], s[0:1], 0x28
	v_readfirstlane_b32 s3, v0
	v_bfe_u32 v70, v0, 4, 2
	v_and_b32_e32 v71, 15, v0
	s_lshr_b32 s3, s3, 6
	s_lshl_b32 s12, s2, 4
	s_lshl_b32 s20, s2, 11
	s_lshl_b32 s21, s3, 7
	s_lshl_b32 s22, s3, 6
	v_lshlrev_b32_e32 v72, 7, v71
	v_lshl_or_b32 v72, v70, 5, v72
	v_lshlrev_b32_e32 v73, 12, v70
	v_lshl_or_b32 v73, v71, 2, v73
	v_lshlrev_b32_e32 v74, 2, v71
	v_lshlrev_b32_e32 v75, 9, v70
	v_lshl_or_b32 v75, v71, 1, v75
	s_add_i32 s23, s22, 0x1080
	v_lshl_add_u32 v76, v70, 4, s23
	s_waitcnt lgkmcnt(0)
	s_load_dword s13, s[16:17], 0x0
	s_add_u32 s4, s4, s20
	s_addc_u32 s5, s5, 0
	s_add_u32 s8, s8, s21
	s_addc_u32 s9, s9, 0
	global_load_dwordx4 v[2:5], v72, s[4:5] nt
	global_load_dwordx4 v[6:9], v72, s[4:5] offset:16 nt
	global_load_dword v26, v73, s[8:9]
	global_load_dword v42, v73, s[8:9] offset:64
	global_load_dword v27, v73, s[8:9] offset:256
	global_load_dword v43, v73, s[8:9] offset:320
	global_load_dword v28, v73, s[8:9] offset:512
	global_load_dword v44, v73, s[8:9] offset:576
	global_load_dword v29, v73, s[8:9] offset:768
	global_load_dword v45, v73, s[8:9] offset:832
	global_load_dword v30, v73, s[8:9] offset:1024
	global_load_dword v46, v73, s[8:9] offset:1088
	global_load_dword v31, v73, s[8:9] offset:1280
	global_load_dword v47, v73, s[8:9] offset:1344
	global_load_dword v32, v73, s[8:9] offset:1536
	global_load_dword v48, v73, s[8:9] offset:1600
	global_load_dword v33, v73, s[8:9] offset:1792
	global_load_dword v49, v73, s[8:9] offset:1856
	global_load_dword v34, v73, s[8:9] offset:2048
	global_load_dword v50, v73, s[8:9] offset:2112
	global_load_dword v35, v73, s[8:9] offset:2304
	global_load_dword v51, v73, s[8:9] offset:2368
	global_load_dword v36, v73, s[8:9] offset:2560
	global_load_dword v52, v73, s[8:9] offset:2624
	global_load_dword v37, v73, s[8:9] offset:2816
	global_load_dword v53, v73, s[8:9] offset:2880
	global_load_dword v38, v73, s[8:9] offset:3072
	global_load_dword v54, v73, s[8:9] offset:3136
	global_load_dword v39, v73, s[8:9] offset:3328
	global_load_dword v55, v73, s[8:9] offset:3392
	global_load_dword v40, v73, s[8:9] offset:3584
	global_load_dword v56, v73, s[8:9] offset:3648
	global_load_dword v41, v73, s[8:9] offset:3840
	global_load_dword v57, v73, s[8:9] offset:3904
	s_add_u32 s6, s6, s20
	s_addc_u32 s7, s7, 0
	s_add_u32 s6, s6, s22
	s_addc_u32 s7, s7, 0
	global_load_ushort v60, v75, s[6:7] nt
	global_load_ushort v64, v75, s[6:7] offset:32 nt
	global_load_ushort v61, v75, s[6:7] offset:128 nt
	global_load_ushort v65, v75, s[6:7] offset:160 nt
	global_load_ushort v62, v75, s[6:7] offset:256 nt
	global_load_ushort v66, v75, s[6:7] offset:288 nt
	global_load_ushort v63, v75, s[6:7] offset:384 nt
	global_load_ushort v67, v75, s[6:7] offset:416 nt
	s_add_u32 s10, s10, s21
	s_addc_u32 s11, s11, 0
	global_load_dword v58, v74, s[10:11]
	global_load_dword v59, v74, s[10:11] offset:64
	s_add_u32 s14, s14, s21
	s_addc_u32 s15, s15, 0
	global_load_dword v68, v74, s[14:15]
	global_load_dword v69, v74, s[14:15] offset:64
	s_lshl_b32 s24, s2, 6
	s_add_u32 s24, s18, s24
	s_addc_u32 s25, s19, 0
	global_load_dword v77, v74, s[24:25]
	v_accvgpr_write_b32 a0, 0
	v_accvgpr_write_b32 a1, 0
	v_accvgpr_write_b32 a2, 0
	v_accvgpr_write_b32 a3, 0
	v_accvgpr_write_b32 a4, 0
	v_accvgpr_write_b32 a5, 0
	v_accvgpr_write_b32 a6, 0
	v_accvgpr_write_b32 a7, 0
	s_waitcnt vmcnt(45)
	v_cvt_f32_f16_e32 v10, v2
	v_cvt_f32_f16_sdwa v11, v2 dst_sel:DWORD dst_unused:UNUSED_PAD src0_sel:WORD_1
	v_cvt_f32_f16_e32 v12, v3
	v_cvt_f32_f16_sdwa v13, v3 dst_sel:DWORD dst_unused:UNUSED_PAD src0_sel:WORD_1
	v_cvt_f32_f16_e32 v14, v4
	v_cvt_f32_f16_sdwa v15, v4 dst_sel:DWORD dst_unused:UNUSED_PAD src0_sel:WORD_1
	v_cvt_f32_f16_e32 v16, v5
	v_cvt_f32_f16_sdwa v17, v5 dst_sel:DWORD dst_unused:UNUSED_PAD src0_sel:WORD_1
	v_cvt_f32_f16_e32 v18, v6
	v_cvt_f32_f16_sdwa v19, v6 dst_sel:DWORD dst_unused:UNUSED_PAD src0_sel:WORD_1
	v_cvt_f32_f16_e32 v20, v7
	v_cvt_f32_f16_sdwa v21, v7 dst_sel:DWORD dst_unused:UNUSED_PAD src0_sel:WORD_1
	v_cvt_f32_f16_e32 v22, v8
	v_cvt_f32_f16_sdwa v23, v8 dst_sel:DWORD dst_unused:UNUSED_PAD src0_sel:WORD_1
	v_cvt_f32_f16_e32 v24, v9
	v_cvt_f32_f16_sdwa v25, v9 dst_sel:DWORD dst_unused:UNUSED_PAD src0_sel:WORD_1
	v_max_f32_e32 v10, 0, v10
	v_max_f32_e32 v11, 0, v11
	v_max_f32_e32 v12, 0, v12
	v_max_f32_e32 v13, 0, v13
	v_max_f32_e32 v14, 0, v14
	v_max_f32_e32 v15, 0, v15
	v_max_f32_e32 v16, 0, v16
	v_max_f32_e32 v17, 0, v17
	v_max_f32_e32 v18, 0, v18
	v_max_f32_e32 v19, 0, v19
	v_max_f32_e32 v20, 0, v20
	v_max_f32_e32 v21, 0, v21
	v_max_f32_e32 v22, 0, v22
	v_max_f32_e32 v23, 0, v23
	v_max_f32_e32 v24, 0, v24
	v_max_f32_e32 v25, 0, v25
	s_waitcnt vmcnt(43)
	v_mfma_f32_16x16x4_f32 a[0:3], v10, v26, a[0:3]
	v_mfma_f32_16x16x4_f32 a[4:7], v10, v42, a[4:7]
	s_waitcnt vmcnt(41)
	v_mfma_f32_16x16x4_f32 a[0:3], v11, v27, a[0:3]
	v_mfma_f32_16x16x4_f32 a[4:7], v11, v43, a[4:7]
	s_waitcnt vmcnt(39)
	v_mfma_f32_16x16x4_f32 a[0:3], v12, v28, a[0:3]
	v_mfma_f32_16x16x4_f32 a[4:7], v12, v44, a[4:7]
	s_waitcnt vmcnt(37)
	v_mfma_f32_16x16x4_f32 a[0:3], v13, v29, a[0:3]
	v_mfma_f32_16x16x4_f32 a[4:7], v13, v45, a[4:7]
	s_waitcnt vmcnt(35)
	v_mfma_f32_16x16x4_f32 a[0:3], v14, v30, a[0:3]
	v_mfma_f32_16x16x4_f32 a[4:7], v14, v46, a[4:7]
	s_waitcnt vmcnt(33)
	v_mfma_f32_16x16x4_f32 a[0:3], v15, v31, a[0:3]
	v_mfma_f32_16x16x4_f32 a[4:7], v15, v47, a[4:7]
	s_waitcnt vmcnt(31)
	v_mfma_f32_16x16x4_f32 a[0:3], v16, v32, a[0:3]
	v_mfma_f32_16x16x4_f32 a[4:7], v16, v48, a[4:7]
	s_waitcnt vmcnt(29)
	v_mfma_f32_16x16x4_f32 a[0:3], v17, v33, a[0:3]
	v_mfma_f32_16x16x4_f32 a[4:7], v17, v49, a[4:7]
	s_waitcnt vmcnt(27)
	v_mfma_f32_16x16x4_f32 a[0:3], v18, v34, a[0:3]
	v_mfma_f32_16x16x4_f32 a[4:7], v18, v50, a[4:7]
	s_waitcnt vmcnt(25)
	v_mfma_f32_16x16x4_f32 a[0:3], v19, v35, a[0:3]
	v_mfma_f32_16x16x4_f32 a[4:7], v19, v51, a[4:7]
	s_waitcnt vmcnt(23)
	v_mfma_f32_16x16x4_f32 a[0:3], v20, v36, a[0:3]
	v_mfma_f32_16x16x4_f32 a[4:7], v20, v52, a[4:7]
	s_waitcnt vmcnt(21)
	v_mfma_f32_16x16x4_f32 a[0:3], v21, v37, a[0:3]
	v_mfma_f32_16x16x4_f32 a[4:7], v21, v53, a[4:7]
	s_waitcnt vmcnt(19)
	v_mfma_f32_16x16x4_f32 a[0:3], v22, v38, a[0:3]
	v_mfma_f32_16x16x4_f32 a[4:7], v22, v54, a[4:7]
	s_waitcnt vmcnt(17)
	v_mfma_f32_16x16x4_f32 a[0:3], v23, v39, a[0:3]
	v_mfma_f32_16x16x4_f32 a[4:7], v23, v55, a[4:7]
	s_waitcnt vmcnt(15)
	v_mfma_f32_16x16x4_f32 a[0:3], v24, v40, a[0:3]
	v_mfma_f32_16x16x4_f32 a[4:7], v24, v56, a[4:7]
	s_waitcnt vmcnt(13)
	v_mfma_f32_16x16x4_f32 a[0:3], v25, v41, a[0:3]
	v_mfma_f32_16x16x4_f32 a[4:7], v25, v57, a[4:7]
	v_cmp_eq_u32_e32 vcc, 0, v71
	s_waitcnt vmcnt(0)
	v_cvt_f32_f16_e32 v60, v60
	v_cvt_f32_f16_e32 v61, v61
	v_cvt_f32_f16_e32 v62, v62
	v_cvt_f32_f16_e32 v63, v63
	v_cvt_f32_f16_e32 v64, v64
	v_cvt_f32_f16_e32 v65, v65
	v_cvt_f32_f16_e32 v66, v66
	v_cvt_f32_f16_e32 v67, v67
	v_add_f32_e32 v60, v58, v60
	v_add_f32_e32 v64, v59, v64
	v_add_f32_e32 v61, v58, v61
	v_add_f32_e32 v65, v59, v65
	v_add_f32_e32 v62, v58, v62
	v_add_f32_e32 v66, v59, v66
	v_add_f32_e32 v63, v58, v63
	v_add_f32_e32 v67, v59, v67
	s_nop 1
	v_accvgpr_read_b32 v2, a0
	v_accvgpr_read_b32 v3, a1
	v_accvgpr_read_b32 v4, a2
	v_accvgpr_read_b32 v5, a3
	v_accvgpr_read_b32 v6, a4
	v_accvgpr_read_b32 v7, a5
	v_accvgpr_read_b32 v8, a6
	v_accvgpr_read_b32 v9, a7
	v_add_f32_e32 v2, v2, v60
	v_add_f32_e32 v3, v3, v61
	v_add_f32_e32 v4, v4, v62
	v_add_f32_e32 v5, v5, v63
	v_add_f32_e32 v6, v6, v64
	v_add_f32_e32 v7, v7, v65
	v_add_f32_e32 v8, v8, v66
	v_add_f32_e32 v9, v9, v67
	v_max_f32_e32 v2, 0, v2
	v_max_f32_e32 v3, 0, v3
	v_max_f32_e32 v4, 0, v4
	v_max_f32_e32 v5, 0, v5
	v_max_f32_e32 v6, 0, v6
	v_max_f32_e32 v7, 0, v7
	v_max_f32_e32 v8, 0, v8
	v_max_f32_e32 v9, 0, v9
	v_mul_f32_e32 v6, v69, v6
	v_mul_f32_e32 v7, v69, v7
	v_mul_f32_e32 v8, v69, v8
	v_mul_f32_e32 v9, v69, v9
	v_fmac_f32_e32 v6, v68, v2
	v_fmac_f32_e32 v7, v68, v3
	v_fmac_f32_e32 v8, v68, v4
	v_fmac_f32_e32 v9, v68, v5
	v_add_f32_dpp v6, v6, v6 quad_perm:[1,0,3,2] row_mask:0xf bank_mask:0xf
	v_add_f32_dpp v7, v7, v7 quad_perm:[1,0,3,2] row_mask:0xf bank_mask:0xf
	v_add_f32_dpp v8, v8, v8 quad_perm:[1,0,3,2] row_mask:0xf bank_mask:0xf
	v_add_f32_dpp v9, v9, v9 quad_perm:[1,0,3,2] row_mask:0xf bank_mask:0xf
	v_add_f32_dpp v6, v6, v6 quad_perm:[2,3,0,1] row_mask:0xf bank_mask:0xf
	v_add_f32_dpp v7, v7, v7 quad_perm:[2,3,0,1] row_mask:0xf bank_mask:0xf
	v_add_f32_dpp v8, v8, v8 quad_perm:[2,3,0,1] row_mask:0xf bank_mask:0xf
	v_add_f32_dpp v9, v9, v9 quad_perm:[2,3,0,1] row_mask:0xf bank_mask:0xf
	v_add_f32_dpp v6, v6, v6 row_half_mirror row_mask:0xf bank_mask:0xf
	v_add_f32_dpp v7, v7, v7 row_half_mirror row_mask:0xf bank_mask:0xf
	v_add_f32_dpp v8, v8, v8 row_half_mirror row_mask:0xf bank_mask:0xf
	v_add_f32_dpp v9, v9, v9 row_half_mirror row_mask:0xf bank_mask:0xf
	v_add_f32_dpp v6, v6, v6 row_mirror row_mask:0xf bank_mask:0xf
	v_add_f32_dpp v7, v7, v7 row_mirror row_mask:0xf bank_mask:0xf
	v_add_f32_dpp v8, v8, v8 row_mirror row_mask:0xf bank_mask:0xf
	v_add_f32_dpp v9, v9, v9 row_mirror row_mask:0xf bank_mask:0xf
	s_and_saveexec_b64 s[2:3], vcc
	ds_write_b128 v76, v[6:9]
	s_or_b64 exec, exec, s[2:3]
	v_cmp_gt_u32_e32 vcc, 16, v0
	s_waitcnt lgkmcnt(0)
	s_barrier
	s_and_saveexec_b64 s[2:3], vcc
	s_cbranch_execz .Lfinal_done
	v_lshlrev_b32_e32 v1, 2, v0
	v_add_u32_e32 v1, 0x1000, v1
	ds_read2_b32 v[2:3], v1 offset0:32 offset1:48
	v_or_b32_e32 v0, s12, v0
	v_ashrrev_i32_e32 v1, 31, v0
	v_lshl_add_u64 v[0:1], v[0:1], 2, s[18:19]
	s_waitcnt lgkmcnt(0)
	v_add_f32_e32 v2, v2, v3
	v_add_f32_e32 v2, s13, v2
	global_store_dword v[0:1], v2, off

	.amdhsa_kernel _Z12final_kernelPKDF16_S0_PKfS2_S2_S2_Pf
		.amdhsa_group_segment_fixed_size 4352
		.amdhsa_private_segment_fixed_size 0
		.amdhsa_kernarg_size 56
		.amdhsa_user_sgpr_count 2
		.amdhsa_user_sgpr_dispatch_ptr 0
		.amdhsa_user_sgpr_queue_ptr 0
		.amdhsa_user_sgpr_kernarg_segment_ptr 1
		.amdhsa_user_sgpr_dispatch_id 0
		.amdhsa_user_sgpr_kernarg_preload_length 0
		.amdhsa_user_sgpr_kernarg_preload_offset 0
		.amdhsa_user_sgpr_private_segment_size 0
		.amdhsa_uses_dynamic_stack 0
		.amdhsa_enable_private_segment 0
		.amdhsa_system_sgpr_workgroup_id_x 1
		.amdhsa_system_sgpr_workgroup_id_y 0
		.amdhsa_system_sgpr_workgroup_id_z 0
		.amdhsa_system_sgpr_workgroup_info 0
		.amdhsa_system_vgpr_workitem_id 0
		.amdhsa_next_free_vgpr 88
		.amdhsa_next_free_sgpr 28
		.amdhsa_accum_offset 80
		.amdhsa_reserve_vcc 1
		.amdhsa_float_round_mode_32 0
		.amdhsa_float_round_mode_16_64 0
		.amdhsa_float_denorm_mode_32 3
		.amdhsa_float_denorm_mode_16_64 3
		.amdhsa_dx10_clamp 1
		.amdhsa_ieee_mode 1
		.amdhsa_fp16_overflow 0
		.amdhsa_tg_split 0
		.amdhsa_exception_fp_ieee_invalid_op 0
		.amdhsa_exception_fp_denorm_src 0
		.amdhsa_exception_fp_ieee_div_zero 0
		.amdhsa_exception_fp_ieee_overflow 0
		.amdhsa_exception_fp_ieee_underflow 0
		.amdhsa_exception_fp_ieee_inexact 0
		.amdhsa_exception_int_div_zero 0
	.end_amdhsa_kernel

amdhsa.kernels:
  - .agpr_count:     8
    .args:
      - .actual_access:  read_only
        .address_space:  global
        .offset:         0
        .size:           8
        .value_kind:     global_buffer
      - .actual_access:  read_only
        .address_space:  global
        .offset:         8
        .size:           8
        .value_kind:     global_buffer
      - .actual_access:  read_only
        .address_space:  global
        .offset:         16
        .size:           8
        .value_kind:     global_buffer
      - .actual_access:  read_only
        .address_space:  global
        .offset:         24
        .size:           8
        .value_kind:     global_buffer
      - .actual_access:  write_only
        .address_space:  global
        .offset:         32
        .size:           8
        .value_kind:     global_buffer
      - .actual_access:  write_only
        .address_space:  global
        .offset:         40
        .size:           8
        .value_kind:     global_buffer
    .group_segment_fixed_size: 4224
    .kernarg_segment_align: 8
    .kernarg_segment_size: 48
    .language:       OpenCL C
    .language_version:
      - 2
      - 0
    .max_flat_workgroup_size: 128
    .name:           _Z11init_kernelPKfS0_S0_S0_PDF16_S1_
    .private_segment_fixed_size: 0
    .sgpr_count:     30
    .sgpr_spill_count: 0
    .symbol:         _Z11init_kernelPKfS0_S0_S0_PDF16_S1_.kd
    .uniform_work_group_size: 1
    .uses_dynamic_stack: false
    .vgpr_count:     68
    .vgpr_spill_count: 0
    .wavefront_size: 64
  - .agpr_count:     8
    .args:
      - .actual_access:  read_only
        .address_space:  global
        .offset:         0
        .size:           8
        .value_kind:     global_buffer
      - .actual_access:  read_only
        .address_space:  global
        .offset:         8
        .size:           8
        .value_kind:     global_buffer
      - .actual_access:  read_only
        .address_space:  global
        .offset:         16
        .size:           8
        .value_kind:     global_buffer
      - .actual_access:  read_only
        .address_space:  global
        .offset:         24
        .size:           8
        .value_kind:     global_buffer
      - .actual_access:  read_only
        .address_space:  global
        .offset:         32
        .size:           8
        .value_kind:     global_buffer
      - .actual_access:  read_only
        .address_space:  global
        .offset:         40
        .size:           8
        .value_kind:     global_buffer
      - .actual_access:  write_only
        .address_space:  global
        .offset:         48
        .size:           8
        .value_kind:     global_buffer
    .group_segment_fixed_size: 4352
    .kernarg_segment_align: 8
    .kernarg_segment_size: 56
    .language:       OpenCL C
    .language_version:
      - 2
      - 0
    .max_flat_workgroup_size: 128
    .name:           _Z12final_kernelPKDF16_S0_PKfS2_S2_S2_Pf
    .private_segment_fixed_size: 0
    .sgpr_count:     34
    .sgpr_spill_count: 0
    .symbol:         _Z12final_kernelPKDF16_S0_PKfS2_S2_S2_Pf.kd
    .uniform_work_group_size: 1
    .uses_dynamic_stack: false
    .vgpr_count:     88
    .vgpr_spill_count: 0
    .wavefront_size: 64
  - .agpr_count:     0
    .args:
      - .actual_access:  read_only
        .address_space:  global
        .offset:         0
        .size:           8
        .value_kind:     global_buffer
      - .actual_access:  read_only
        .address_space:  global
        .offset:         8
        .size:           8
        .value_kind:     global_buffer
      - .actual_access:  read_only
        .address_space:  global
        .offset:         16
        .size:           8
        .value_kind:     global_buffer
      - .actual_access:  read_only
        .address_space:  global
        .offset:         24
        .size:           8
        .value_kind:     global_buffer
      - .actual_access:  read_only
        .address_space:  global
        .offset:         32
        .size:           8
        .value_kind:     global_buffer
      - .actual_access:  read_only
        .address_space:  global
        .offset:         40
        .size:           8
        .value_kind:     global_buffer
      - .actual_access:  read_only
        .address_space:  global
        .offset:         48
        .size:           8
        .value_kind:     global_buffer
      - .actual_access:  read_only
        .address_space:  global
        .offset:         56
        .size:           8
        .value_kind:     global_buffer
      - .actual_access:  read_only
        .address_space:  global
        .offset:         64
        .size:           8
        .value_kind:     global_buffer
      - .actual_access:  read_only
        .address_space:  global
        .offset:         72
        .size:           8
        .value_kind:     global_buffer
      - .address_space:  global
        .offset:         80
        .size:           8
        .value_kind:     global_buffer
    .group_segment_fixed_size: 16896
    .kernarg_segment_align: 8
    .kernarg_segment_size: 88
    .language:       OpenCL C
    .language_version:
      - 2
      - 0
    .max_flat_workgroup_size: 128
    .name:           _Z11edge_kernelILi36ELb1EEvPKfS1_PKDF16_PKiS5_S1_S1_S1_S1_S1_PDF16_
    .private_segment_fixed_size: 0
    .sgpr_count:     45
    .sgpr_spill_count: 0
    .symbol:         _Z11edge_kernelILi36ELb1EEvPKfS1_PKDF16_PKiS5_S1_S1_S1_S1_S1_PDF16_.kd
    .uniform_work_group_size: 1
    .uses_dynamic_stack: false
    .vgpr_count:     168
    .vgpr_spill_count: 0
    .wavefront_size: 64
  - .agpr_count:     0
    .args:
      - .actual_access:  read_only
        .address_space:  global
        .offset:         0
        .size:           8
        .value_kind:     global_buffer
      - .actual_access:  read_only
        .address_space:  global
        .offset:         8
        .size:           8
        .value_kind:     global_buffer
      - .actual_access:  read_only
        .address_space:  global
        .offset:         16
        .size:           8
        .value_kind:     global_buffer
      - .actual_access:  read_only
        .address_space:  global
        .offset:         24
        .size:           8
        .value_kind:     global_buffer
      - .actual_access:  read_only
        .address_space:  global
        .offset:         32
        .size:           8
        .value_kind:     global_buffer
      - .actual_access:  read_only
        .address_space:  global
        .offset:         40
        .size:           8
        .value_kind:     global_buffer
      - .actual_access:  read_only
        .address_space:  global
        .offset:         48
        .size:           8
        .value_kind:     global_buffer
      - .actual_access:  read_only
        .address_space:  global
        .offset:         56
        .size:           8
        .value_kind:     global_buffer
      - .actual_access:  read_only
        .address_space:  global
        .offset:         64
        .size:           8
        .value_kind:     global_buffer
      - .actual_access:  read_only
        .address_space:  global
        .offset:         72
        .size:           8
        .value_kind:     global_buffer
      - .address_space:  global
        .offset:         80
        .size:           8
        .value_kind:     global_buffer
    .group_segment_fixed_size: 16896
    .kernarg_segment_align: 8
    .kernarg_segment_size: 88
    .language:       OpenCL C
    .language_version:
      - 2
      - 0
    .max_flat_workgroup_size: 128
    .name:           _Z11edge_kernelILi64ELb0EEvPKfS1_PKDF16_PKiS5_S1_S1_S1_S1_S1_PDF16_
    .private_segment_fixed_size: 0
    .sgpr_count:     44
    .sgpr_spill_count: 0
    .symbol:         _Z11edge_kernelILi64ELb0EEvPKfS1_PKDF16_PKiS5_S1_S1_S1_S1_S1_PDF16_.kd
    .uniform_work_group_size: 1
    .uses_dynamic_stack: false
    .vgpr_count:     168
    .vgpr_spill_count: 0
    .wavefront_size: 64
